# MoE: expert-count table loads and per-tile idx gathers issued together with one wait instead of serialized waits
# speedup vs baseline: 1.0117x; 1.0051x over previous
; #define LAS __attribute__((address_space(3)))
; __device__ __forceinline__ void moe_table(Frame& F) {
;     LAS int* tab = (LAS int*)(F.lds + MOETAB_OFF);
;     __syncthreads();
;     if (F.tid == 0) { int cum = 0; for (int e = 0; e < NE; ++e) { const int cn = (int)__hip_atomic_load(F.ctl + CW_CNT + e, __ATOMIC_RELAXED, __HIP_MEMORY_SCOPE_AGENT); tab[e] = cn; tab[8 + e] = cum; cum += (cn + 255) >> 8; } tab[16] = cum; }
;     __syncthreads();
; }
.LBB0_2252:
	v_readlane_b32 s0, v255, 11
	v_readlane_b32 s1, v255, 12
	s_cmp_lt_i32 s0, 16
	s_cselect_b64 s[0:1], -1, 0
	s_and_b64 s[4:5], s[0:1], s[6:7]
	s_andn2_b64 vcc, exec, s[4:5]
	s_cbranch_vccnz .LBB0_2317
	s_waitcnt vmcnt(0) lgkmcnt(0)
	s_barrier
	s_mov_b64 s[6:7], exec
	v_readlane_b32 s4, v255, 7
	v_readlane_b32 s5, v255, 8
	s_and_b64 s[4:5], s[6:7], s[4:5]
	s_mov_b64 exec, s[4:5]
	s_cbranch_execz .LBB0_2255
	v_mov_b32_e32 v1, 0
	global_load_dwordx4 v[2:5], v1, s[50:51] offset:256 sc1
	global_load_dwordx4 v[6:9], v1, s[50:51] offset:272 sc1
	s_add_i32 s3, 0, 0x20040
	v_mov_b32_e32 v18, s3
	s_waitcnt vmcnt(0)
	ds_write_b128 v18, v[2:5]
	ds_write_b128 v18, v[6:9] offset:16
	v_mov_b32_e32 v10, 0
	s_nop 1
	v_add_u32_e32 v2, 0xff, v2
	v_ashrrev_i32_e32 v2, 8, v2
	v_add_u32_e32 v3, 0xff, v3
	v_ashrrev_i32_e32 v3, 8, v3
	v_add_u32_e32 v4, 0xff, v4
	v_ashrrev_i32_e32 v4, 8, v4
	v_add_u32_e32 v5, 0xff, v5
	v_ashrrev_i32_e32 v5, 8, v5
	v_add_u32_e32 v6, 0xff, v6
	v_ashrrev_i32_e32 v6, 8, v6
	v_add_u32_e32 v7, 0xff, v7
	v_ashrrev_i32_e32 v7, 8, v7
	v_add_u32_e32 v8, 0xff, v8
	v_ashrrev_i32_e32 v8, 8, v8
	v_add_u32_e32 v9, 0xff, v9
	v_ashrrev_i32_e32 v9, 8, v9
	v_mov_b32_e32 v11, v2
	v_add_u32_e32 v12, v11, v3
	v_add_u32_e32 v13, v12, v4
	v_add_u32_e32 v14, v13, v5
	v_add_u32_e32 v15, v14, v6
	v_add_u32_e32 v16, v15, v7
	v_add_u32_e32 v17, v16, v8
	v_add_u32_e32 v1, v17, v9
	ds_write_b128 v18, v[10:13] offset:32
	ds_write_b128 v18, v[14:17] offset:48
	ds_write_b32 v18, v1 offset:64

;     __device__ __forceinline__ void a_offsets(const Unit& u, const int (&Rr)[2], const int (&Cc)[2], unsigned (&off)[2][2]) const {
;         const int cume = tab[8 + u.e], cnte = tab[u.e];
; #pragma unroll
;         for (int h = 0; h < 2; ++h)
; #pragma unroll
;             for (int i = 0; i < 2; ++i) {
;                 if (GATHER_) { const int rl = (u.pm - cume) * BM + h * HALF + Rr[i]; const int tok = (rl < cnte) ? idx[u.e * ECAP + rl] : 0; off[h][i] = (unsigned)(tok * KB + Cc[i] * 2); }
;                 else off[h][i] = (unsigned)((u.pm * BM + h * HALF + Rr[i]) * KB + Cc[i] * 2);
;             }
;     }
.LBB0_2281:
	s_nop 0
	v_cndmask_b32_e64 v4, 0, 1, s[8:9]
	v_cmp_ne_u32_e64 s[6:7], 1, v4
	s_andn2_b64 vcc, exec, s[8:9]
	v_mov_b32_e32 v173, v81
	v_mov_b32_e32 v174, v80
	v_mov_b32_e32 v175, v78
	v_mov_b32_e32 v176, v86
	s_cbranch_vccnz .LBB0_2291
	v_lshlrev_b32_e32 v4, 2, v172
	v_add_u32_e32 v4, 0, v4
	v_add_u32_e32 v4, 0x20040, v4
	ds_read2_b32 v[4:5], v4 offset1:8
	v_mov_b32_e32 v6, 0
	s_waitcnt lgkmcnt(0)
	v_sub_u32_e32 v5, s71, v5
	v_lshlrev_b32_e32 v7, 8, v5
	v_or_b32_e32 v8, v7, v1
	v_cmp_lt_i32_e32 vcc, v8, v4
	v_mov_b32_e32 v5, 0
	s_and_saveexec_b64 s[8:9], vcc
	s_cbranch_execz .LBB0_2284
	v_lshl_add_u32 v8, v172, 14, v8
	v_ashrrev_i32_e32 v9, 31, v8
	v_lshl_add_u64 v[8:9], v[8:9], 2, s[30:31]
	global_load_dword v5, v[8:9], off
.LBB0_2284:
	s_or_b64 exec, exec, s[8:9]
	v_or_b32_e32 v8, v7, v163
	v_cmp_lt_i32_e32 vcc, v8, v4
	s_and_saveexec_b64 s[8:9], vcc
	s_cbranch_execz .LBB0_2286
	v_lshl_add_u32 v8, v172, 14, v8
	v_ashrrev_i32_e32 v9, 31, v8
	v_lshl_add_u64 v[8:9], v[8:9], 2, s[30:31]
	global_load_dword v6, v[8:9], off
.LBB0_2286:
	s_or_b64 exec, exec, s[8:9]
	v_or_b32_e32 v9, 0x80, v7
	v_or_b32_e32 v10, v9, v1
	v_cmp_lt_i32_e32 vcc, v10, v4
	v_mov_b32_e32 v7, 0
	v_mov_b32_e32 v8, 0
	s_and_saveexec_b64 s[8:9], vcc
	s_cbranch_execz .LBB0_2288
	v_lshl_add_u32 v10, v172, 14, v10
	v_ashrrev_i32_e32 v11, 31, v10
	v_lshl_add_u64 v[10:11], v[10:11], 2, s[30:31]
	global_load_dword v8, v[10:11], off
.LBB0_2288:
	s_or_b64 exec, exec, s[8:9]
	v_add_u32_e32 v9, v9, v163
	v_cmp_lt_i32_e32 vcc, v9, v4
	s_and_saveexec_b64 s[8:9], vcc
	s_cbranch_execz .LBB0_2290
	v_lshl_add_u32 v10, v172, 14, v9
	v_ashrrev_i32_e32 v11, 31, v10
	v_lshl_add_u64 v[10:11], v[10:11], 2, s[30:31]
	global_load_dword v4, v[10:11], off
	s_waitcnt vmcnt(0)
	v_lshlrev_b32_e32 v7, 11, v4
.LBB0_2290:
	s_or_b64 exec, exec, s[8:9]
	s_waitcnt vmcnt(0)
	v_lshlrev_b32_e32 v5, 11, v5
	v_lshlrev_b32_e32 v6, 11, v6
	v_lshlrev_b32_e32 v8, 11, v8
	v_or_b32_e32 v175, v8, v164
	v_or_b32_e32 v174, v6, v164
	v_or_b32_e32 v173, v5, v164
	v_or_b32_e32 v176, v7, v164

; #define LAS __attribute__((address_space(3)))
; __device__ __forceinline__ void moe_table(Frame& F) {
;     LAS int* tab = (LAS int*)(F.lds + MOETAB_OFF);
;     __syncthreads();
;     if (F.tid == 0) { int cum = 0; for (int e = 0; e < NE; ++e) { const int cn = (int)__hip_atomic_load(F.ctl + CW_CNT + e, __ATOMIC_RELAXED, __HIP_MEMORY_SCOPE_AGENT); tab[e] = cn; tab[8 + e] = cum; cum += (cn + 255) >> 8; } tab[16] = cum; }
;     __syncthreads();
; }
.LBB0_2371:
	v_readlane_b32 s0, v255, 11
	v_readlane_b32 s1, v255, 12
	s_cmp_lt_i32 s0, 17
	s_cselect_b64 s[0:1], -1, 0
	s_and_b64 s[4:5], s[0:1], s[6:7]
	s_andn2_b64 vcc, exec, s[4:5]
	s_cbranch_vccnz .LBB0_2394
	s_waitcnt vmcnt(0) lgkmcnt(0)
	s_barrier
	s_mov_b64 s[6:7], exec
	v_readlane_b32 s4, v255, 7
	v_readlane_b32 s5, v255, 8
	s_and_b64 s[4:5], s[6:7], s[4:5]
	s_mov_b64 exec, s[4:5]
	s_cbranch_execz .LBB0_2374
	v_mov_b32_e32 v1, 0
	global_load_dwordx4 v[2:5], v1, s[50:51] offset:256 sc1
	global_load_dwordx4 v[6:9], v1, s[50:51] offset:272 sc1
	s_add_i32 s3, 0, 0x20040
	v_mov_b32_e32 v18, s3
	s_waitcnt vmcnt(0)
	ds_write_b128 v18, v[2:5]
	ds_write_b128 v18, v[6:9] offset:16
	v_mov_b32_e32 v10, 0
	s_nop 1
	v_add_u32_e32 v2, 0xff, v2
	v_ashrrev_i32_e32 v2, 8, v2
	v_add_u32_e32 v3, 0xff, v3
	v_ashrrev_i32_e32 v3, 8, v3
	v_add_u32_e32 v4, 0xff, v4
	v_ashrrev_i32_e32 v4, 8, v4
	v_add_u32_e32 v5, 0xff, v5
	v_ashrrev_i32_e32 v5, 8, v5
	v_add_u32_e32 v6, 0xff, v6
	v_ashrrev_i32_e32 v6, 8, v6
	v_add_u32_e32 v7, 0xff, v7
	v_ashrrev_i32_e32 v7, 8, v7
	v_add_u32_e32 v8, 0xff, v8
	v_ashrrev_i32_e32 v8, 8, v8
	v_add_u32_e32 v9, 0xff, v9
	v_ashrrev_i32_e32 v9, 8, v9
	v_mov_b32_e32 v11, v2
	v_add_u32_e32 v12, v11, v3
	v_add_u32_e32 v13, v12, v4
	v_add_u32_e32 v14, v13, v5
	v_add_u32_e32 v15, v14, v6
	v_add_u32_e32 v16, v15, v7
	v_add_u32_e32 v17, v16, v8
	v_add_u32_e32 v1, v17, v9
	ds_write_b128 v18, v[10:13] offset:32
	ds_write_b128 v18, v[14:17] offset:48
	ds_write_b32 v18, v1 offset:64

; template <int YMODE, int EXTRA, bool NORM_OUT, bool XN8  , bool XIN_BF = false  , bool XOUT_BF = false  > ...
;     ...
;     if (YMODE == 2) { if (F.tid == 0) { int cum = 0; for (int e = 0; e < NE; ++e) { cumt[e] = cum; cum += (int)((__hip_atomic_load(cntw + e, __ATOMIC_RELAXED, __HIP_MEMORY_SCOPE_AGENT) + 255u) >> 8); } } }
.LBB0_2448:
	v_readlane_b32 s0, v255, 11
	v_readlane_b32 s1, v255, 12
	s_cmp_gt_i32 s0, 17
	s_cselect_b64 s[0:1], -1, 0
	s_xor_b64 s[4:5], s[6:7], -1
	s_or_b64 s[0:1], s[0:1], s[4:5]
	s_and_b64 vcc, exec, s[0:1]
	s_cbranch_vccnz .LBB0_2459
	s_add_i32 s0, 0, 0x20238
	s_waitcnt vmcnt(0)
	v_mov_b32_e32 v1, s0
	s_waitcnt lgkmcnt(3)
	ds_read_b64 v[2:3], v1
	s_waitcnt lgkmcnt(0)
	v_readfirstlane_b32 s0, v2
	v_readfirstlane_b32 s1, v3
	s_mov_b64 s[6:7], exec
	v_readlane_b32 s4, v255, 7
	v_readlane_b32 s5, v255, 8
	s_and_b64 s[4:5], s[6:7], s[4:5]
	s_mov_b64 exec, s[4:5]
	s_cbranch_execz .LBB0_2451
	v_mov_b32_e32 v1, 0
	global_load_dwordx4 v[2:5], v1, s[50:51] offset:256 sc1
	global_load_dwordx4 v[6:9], v1, s[50:51] offset:272 sc1
	s_add_i32 s3, 0, 0x16800
	v_mov_b32_e32 v18, s3
	v_mov_b32_e32 v10, 0
	s_waitcnt vmcnt(0)
	v_add_u32_e32 v2, 0xff, v2
	v_lshrrev_b32_e32 v2, 8, v2
	v_add_u32_e32 v3, 0xff, v3
	v_lshrrev_b32_e32 v3, 8, v3
	v_add_u32_e32 v4, 0xff, v4
	v_lshrrev_b32_e32 v4, 8, v4
	v_add_u32_e32 v5, 0xff, v5
	v_lshrrev_b32_e32 v5, 8, v5
	v_add_u32_e32 v6, 0xff, v6
	v_lshrrev_b32_e32 v6, 8, v6
	v_add_u32_e32 v7, 0xff, v7
	v_lshrrev_b32_e32 v7, 8, v7
	v_add_u32_e32 v8, 0xff, v8
	v_lshrrev_b32_e32 v8, 8, v8
	v_mov_b32_e32 v11, v2
	v_add_u32_e32 v12, v11, v3
	v_add_u32_e32 v13, v12, v4
	v_add_u32_e32 v14, v13, v5
	v_add_u32_e32 v15, v14, v6
	v_add_u32_e32 v16, v15, v7
	v_add_u32_e32 v17, v16, v8
	ds_write_b128 v18, v[10:13]
	ds_write_b128 v18, v[14:17] offset:16
